# scan loader: nt hint also on the 4 bf16 weight-tile stores
# baseline (speedup 1.0000x reference)
; #define LAS __attribute__((address_space(3)))
; __device__ __forceinline__ unsigned cvt_pk_bf16(float lo, float hi) { unsigned r; asm volatile("v_cvt_pk_bf16_f32 %0, %1, %2" : "=v"(r) : "v"(lo), "v"(hi)); return r; }
; __device__ __forceinline__ void p4_scan(const Args& a, const Frame& F) {
;     ...
;             auto commitK = [&](int kbuf) {
; #pragma unroll
;                 for (int i = 0; i < 8; ++i) { const int p = ht + 256 * i, row = p >> 4, c16 = p & 15; *(LAS u32x4*)(L + kbuf + row * SP + c16 * 16) = pk[i]; } };
;     ...
;             auto conv_store = [&]() {
;                 const bool hi = lane >= 32;
;                 u32x4 o[4];
; #pragma unroll
;                 for (int i = 0; i < 16; ++i) { const float snd = hi ? cv[i] : cv[16 + i]; const float rcv = __shfl_xor(snd, 32);
;                     const unsigned pkd = pg8::cvt_pk_bf16(hi ? rcv : cv[i], hi ? cv[16 + i] : rcv);
;                     if ((i & 3) == 0) o[i >> 2].x = pkd; else if ((i & 3) == 1) o[i >> 2].y = pkd; else if ((i & 3) == 2) o[i >> 2].z = pkd; else o[i >> 2].w = pkd; }
;                 u32x4* dst = (u32x4*)(cD + (size_t)crow * 1024 + ck0 + (hi ? 32 : 0));
; #pragma unroll
;                 for (int j2 = 0; j2 < 4; ++j2) dst[j2] = o[j2];
;             };
.LBB0_496:
	s_or_b64 exec, exec, s[54:55]
	s_ashr_i32 s54, s56, 7
	s_add_i32 s54, s54, s76
	s_lshl_b32 s54, s54, 1
	s_ashr_i32 s55, s54, 31
	s_lshl_b64 s[54:55], s[54:55], 2
	s_add_u32 s54, s60, s54
	s_addc_u32 s55, s61, s55
	global_load_dwordx2 v[94:95], v145, s[54:55]
	s_bitcmp0_b32 s44, 0
	s_cselect_b64 s[54:55], -1, 0
	s_and_b64 s[56:57], s[54:55], exec
	s_cselect_b32 s56, 0x11000, s91
	s_add_i32 s56, s56, 0
	v_add3_u32 v144, s56, v109, v117
	ds_write_b128 v144, v[220:223]
	v_add3_u32 v48, s56, v110, v117
	ds_write_b128 v48, v[224:227]
	v_add3_u32 v48, s56, v111, v117
	ds_write_b128 v48, v[228:231]
	v_add3_u32 v48, s56, v112, v117
	ds_write_b128 v48, v[232:235]
	v_add3_u32 v48, s56, v113, v117
	ds_write_b128 v48, v[236:239]
	v_add3_u32 v48, s56, v114, v117
	ds_write_b128 v48, v[240:243]
	v_add3_u32 v48, s56, v115, v117
	ds_write_b128 v48, v[244:247]
	v_add3_u32 v48, s56, v116, v117
	ds_write_b128 v48, v[248:251]
	s_add_i32 s98, s35, 1
	s_min_i32 s98, s98, 0x41
	s_sub_i32 s99, 0x41, s98
	s_add_i32 s98, s98, -2
	s_and_b64 s[100:101], s[4:5], exec
	s_cselect_b32 s98, s98, s99
	s_lshl_b32 s98, s98, 7
	s_add_i32 s98, s98, s33
	v_add_u32_e32 v214, s98, v96
	v_ashrrev_i32_e32 v215, 31, v214
	v_lshlrev_b64 v[214:215], 11, v[214:215]
	v_lshl_add_u64 v[214:215], v[92:93], 0, v[214:215]
	global_load_dwordx4 v[220:223], v[214:215], off offset:1024
	v_add_u32_e32 v214, s98, v97
	v_ashrrev_i32_e32 v215, 31, v214
	v_lshlrev_b64 v[214:215], 11, v[214:215]
	v_lshl_add_u64 v[214:215], v[92:93], 0, v[214:215]
	global_load_dwordx4 v[224:227], v[214:215], off offset:1024
	v_add_u32_e32 v214, s98, v98
	v_ashrrev_i32_e32 v215, 31, v214
	v_lshlrev_b64 v[214:215], 11, v[214:215]
	v_lshl_add_u64 v[214:215], v[92:93], 0, v[214:215]
	global_load_dwordx4 v[228:231], v[214:215], off offset:1024
	v_add_u32_e32 v214, s98, v99
	v_ashrrev_i32_e32 v215, 31, v214
	v_lshlrev_b64 v[214:215], 11, v[214:215]
	v_lshl_add_u64 v[214:215], v[92:93], 0, v[214:215]
	global_load_dwordx4 v[232:235], v[214:215], off offset:1024
	v_add_u32_e32 v214, s98, v100
	v_ashrrev_i32_e32 v215, 31, v214
	v_lshlrev_b64 v[214:215], 11, v[214:215]
	v_lshl_add_u64 v[214:215], v[92:93], 0, v[214:215]
	global_load_dwordx4 v[236:239], v[214:215], off offset:1024
	v_add_u32_e32 v214, s98, v101
	v_ashrrev_i32_e32 v215, 31, v214
	v_lshlrev_b64 v[214:215], 11, v[214:215]
	v_lshl_add_u64 v[214:215], v[92:93], 0, v[214:215]
	global_load_dwordx4 v[240:243], v[214:215], off offset:1024
	v_add_u32_e32 v214, s98, v102
	v_ashrrev_i32_e32 v215, 31, v214
	v_lshlrev_b64 v[214:215], 11, v[214:215]
	v_lshl_add_u64 v[214:215], v[92:93], 0, v[214:215]
	global_load_dwordx4 v[244:247], v[214:215], off offset:1024
	v_add_u32_e32 v214, s98, v103
	v_ashrrev_i32_e32 v215, 31, v214
	v_lshlrev_b64 v[214:215], 11, v[214:215]
	v_lshl_add_u64 v[214:215], v[92:93], 0, v[214:215]
	global_load_dwordx4 v[248:251], v[214:215], off offset:1024
	s_waitcnt vmcnt(21)
	s_cmp_gt_u32 s44, 47
	s_cbranch_scc1 .LBB0_498
	v_cvt_pk_bf16_f32 v48, v174, v178
	v_cvt_pk_bf16_f32 v49, v182, v138
	v_cvt_pk_bf16_f32 v50, v148, v198
	v_cvt_pk_bf16_f32 v51, v202, v210
	v_cvt_pk_bf16_f32 v52, v175, v179
	v_cvt_pk_bf16_f32 v53, v183, v139
	v_cvt_pk_bf16_f32 v54, v149, v199
	v_cvt_pk_bf16_f32 v55, v203, v211
	v_cvt_pk_bf16_f32 v56, v176, v180
	v_cvt_pk_bf16_f32 v57, v184, v140
	v_cvt_pk_bf16_f32 v58, v150, v200
	v_cvt_pk_bf16_f32 v59, v204, v212
	v_cvt_pk_bf16_f32 v60, v177, v181
	v_cvt_pk_bf16_f32 v61, v185, v141
	v_cvt_pk_bf16_f32 v62, v151, v201
	v_cvt_pk_bf16_f32 v63, v205, v213
	v_add_u32_e32 v80, v80, v206
	v_ashrrev_i32_e32 v81, 31, v80
	v_lshlrev_b64 v[64:65], 11, v[80:81]
	v_lshl_add_u64 v[64:65], s[52:53], 0, v[64:65]
	v_add_u32_e32 v82, v82, v207
	v_mov_b32_e32 v83, v145
	v_lshl_add_u64 v[64:65], v[82:83], 1, v[64:65]
	s_mov_b64 s[100:101], 0x1000
	global_store_dwordx4 v[64:65], v[48:51], off nt
	global_store_dwordx4 v[64:65], v[52:55], off offset:2048 nt
	s_nop 1
	v_lshl_add_u64 v[64:65], s[100:101], 0, v[64:65]
	global_store_dwordx4 v[64:65], v[56:59], off nt
	global_store_dwordx4 v[64:65], v[60:63], off offset:2048 nt
